# v040 plus MFMA-first at GQA step head and static s_setprio 1 for waves 4-7 during attention
# baseline (speedup 1.0000x reference)
.LBB0_871:
	s_cmp_ge_i32 s36, s28
	s_cselect_b64 s[6:7], -1, 0
	s_and_b64 s[4:5], s[6:7], s[4:5]
	s_andn2_b64 vcc, exec, s[4:5]
	s_cbranch_vccnz .LBB0_1055
	v_readfirstlane_b32 s4, v0
	s_nop 0
	s_bitcmp1_b32 s4, 8
	s_cbranch_scc0 .Lprio_att
	s_setprio 1
.Lprio_att:
	s_load_dwordx2 s[14:15], s[74:75], 0xd8
	v_mov_b32_e32 v1, v0
	v_readlane_b32 s4, v254, 3
	v_and_b32_e32 v208, 31, v1
	s_waitcnt lgkmcnt(0)
	s_add_u32 s62, s14, 0x1ca00000
	s_addc_u32 s63, s15, 0
	s_add_u32 s66, s14, 0x2b100000
	s_addc_u32 s67, s15, 0
	s_add_u32 s68, s14, 0x2e280000
	v_bfe_u32 v250, v1, 5, 1
	s_addc_u32 s69, s15, 0
	v_lshlrev_b32_e32 v4, 10, v250
	v_lshlrev_b32_e32 v6, 4, v208
	s_add_u32 s70, s14, 0x31400000
	v_lshlrev_b32_e32 v5, 3, v1
	v_add3_u32 v253, 0, v4, v6
	v_lshlrev_b32_e32 v4, 1, v1
	s_addc_u32 s71, s15, 0
	v_and_b32_e32 v214, 24, v5
	v_and_b32_e32 v4, 32, v4
	v_lshlrev_b32_e32 v211, 4, v1
	s_add_u32 s72, s14, 0x18800000
	v_add3_u32 v4, 0, v4, v214
	v_lshlrev_b32_e32 v6, 8, v250
	v_and_b32_e32 v7, 0xc0, v211
	v_readlane_b32 s5, v254, 4
	s_addc_u32 s73, s15, 0
	v_add3_u32 v242, v4, v6, v7
	v_bfe_u32 v7, v1, 3, 3
	s_load_dword s60, s[4:5], 0x0
	v_readlane_b32 s61, v254, 0
	s_add_u32 s74, s14, 0x1a900000
	v_and_b32_e32 v212, 56, v5
	v_or_b32_e32 v5, 8, v7
	s_waitcnt lgkmcnt(0)
	s_addc_u32 s75, s15, 0
	s_ashr_i32 s96, s60, 31
	s_ashr_i32 s97, s61, 31
	v_lshlrev_b32_e32 v249, 7, v5
	v_lshlrev_b32_e32 v8, 9, v5
	v_or_b32_e32 v5, 16, v7
	v_and_b32_e32 v251, 63, v1
	s_and_b64 s[4:5], s[64:65], exec
	v_lshlrev_b32_e32 v240, 7, v5
	v_lshlrev_b32_e32 v10, 9, v5
	v_or_b32_e32 v5, 24, v7
	v_writelane_b32 v255, s6, 27
	s_movk_i32 s4, 0x800
	s_mov_b32 s17, 0
	v_mul_u32_u24_e32 v2, 0x300, v251
	v_mul_u32_u24_e32 v4, 0x300, v208
	v_lshlrev_b32_e32 v6, 9, v7
	v_lshlrev_b32_e32 v12, 9, v5
	v_mul_u32_u24_e32 v14, 0xe00, v251
	v_mul_u32_u24_e32 v16, 0xe00, v208
	v_writelane_b32 v255, s7, 28
	s_cselect_b32 s16, s4, 0x840
	v_bfe_u32 v252, v1, 2, 4
	v_cmp_gt_u32_e64 s[4:5], 32, v251
	v_lshlrev_b32_e32 v210, 3, v250
	v_lshlrev_b32_e32 v209, 4, v250
	v_lshlrev_b32_e32 v248, 9, v250
	v_lshlrev_b32_e32 v245, 7, v7
	v_lshlrev_b32_e32 v246, 7, v5
	v_cmp_eq_u32_e64 s[6:7], 0, v251
	v_lshlrev_b32_e32 v216, 1, v2
	v_lshlrev_b32_e32 v218, 1, v4
	v_lshlrev_b32_e32 v220, 1, v6
	v_lshlrev_b32_e32 v222, 1, v8
	v_lshlrev_b32_e32 v224, 1, v10
	v_lshlrev_b32_e32 v226, 1, v12
	v_lshlrev_b32_e32 v228, 1, v14
	v_lshlrev_b32_e32 v230, 1, v16
	s_mov_b32 s76, s17
	s_branch .LBB0_875

.LBB0_910:
	s_mov_b32 s40, s13
	s_mov_b32 s8, s24
	s_mov_b32 s9, s39
	v_add_u32_e32 v2, s11, v242
	ds_read_b64_tr_b16 v[172:173], v2 offset:24576
	ds_read_b64_tr_b16 v[174:175], v2 offset:25088
	v_mfma_f32_32x32x16_bf16 v[84:99], v[160:163], v[112:115], 0
	v_add_f32_e32 v68, v52, v53
	v_add_f32_e32 v68, v54, v68
	v_add_f32_e32 v68, v55, v68
	v_add_f32_e32 v68, v56, v68
	v_add_f32_e32 v68, v57, v68
	v_cvt_pk_bf16_f32 v128, v52, v53
	v_cvt_pk_bf16_f32 v129, v54, v55
	ds_read_b64_tr_b16 v[52:53], v2 offset:28672
	ds_read_b64_tr_b16 v[54:55], v2 offset:29184
	v_add_f32_e32 v68, v58, v68
	v_add_f32_e32 v68, v59, v68
	v_add_f32_e32 v68, v60, v68
	v_add_f32_e32 v116, v61, v68
	v_cvt_pk_bf16_f32 v130, v56, v57
	v_cvt_pk_bf16_f32 v131, v58, v59
	s_waitcnt lgkmcnt(10)
	v_mfma_f32_32x32x16_bf16 v[68:83], v[152:155], v[112:115], 0
	ds_read_b64_tr_b16 v[56:57], v2 offset:25600
	ds_read_b64_tr_b16 v[58:59], v2 offset:26112
	v_add_f32_e32 v116, v62, v116
	v_add_f32_e32 v116, v63, v116
	v_add_f32_e32 v116, v64, v116
	v_add_f32_e32 v116, v65, v116
	v_cvt_pk_bf16_f32 v124, v60, v61
	v_cvt_pk_bf16_f32 v125, v62, v63
	s_waitcnt lgkmcnt(11)
	v_mfma_f32_32x32x16_bf16 v[84:99], v[156:159], v[108:111], v[84:99]
	ds_read_b64_tr_b16 v[60:61], v2 offset:29696
	ds_read_b64_tr_b16 v[62:63], v2 offset:30208
	v_add_f32_e32 v116, v66, v116
	v_add_f32_e32 v116, v67, v116
	v_add_f32_e32 v116, v36, v116
	v_add_f32_e32 v116, v37, v116
	v_cvt_pk_bf16_f32 v126, v64, v65
	v_cvt_pk_bf16_f32 v127, v66, v67
	s_waitcnt lgkmcnt(12)
	v_mfma_f32_32x32x16_bf16 v[68:83], v[148:151], v[108:111], v[68:83]
	ds_read_b64_tr_b16 v[64:65], v2 offset:26624
	ds_read_b64_tr_b16 v[66:67], v2 offset:27136
	v_add_f32_e32 v116, v38, v116
	v_add_f32_e32 v116, v39, v116
	v_add_f32_e32 v116, v40, v116
	v_add_f32_e32 v116, v41, v116
	v_cvt_pk_bf16_f32 v120, v36, v37
	v_cvt_pk_bf16_f32 v121, v38, v39
	s_waitcnt lgkmcnt(13)
	v_mfma_f32_32x32x16_bf16 v[84:99], v[144:147], v[104:107], v[84:99]
	ds_read_b64_tr_b16 v[36:37], v2 offset:30720
	ds_read_b64_tr_b16 v[38:39], v2 offset:31232
	v_add_f32_e32 v116, v42, v116
	v_add_f32_e32 v116, v43, v116
	v_add_f32_e32 v116, v44, v116
	v_add_f32_e32 v116, v45, v116
	v_cvt_pk_bf16_f32 v122, v40, v41
	v_cvt_pk_bf16_f32 v123, v42, v43
	s_waitcnt lgkmcnt(14)
	v_mfma_f32_32x32x16_bf16 v[68:83], v[140:143], v[104:107], v[68:83]
	ds_read_b64_tr_b16 v[40:41], v2 offset:27648
	ds_read_b64_tr_b16 v[42:43], v2 offset:28160
	v_add_f32_e32 v116, v46, v116
	v_add_f32_e32 v116, v47, v116
	v_add_f32_e32 v116, v48, v116
	s_waitcnt lgkmcnt(14)
	v_mfma_f32_32x32x16_bf16 v[84:99], v[136:139], v[100:103], v[84:99]
	v_add_f32_e32 v136, v49, v116
	v_cvt_pk_bf16_f32 v116, v44, v45
	v_cvt_pk_bf16_f32 v117, v46, v47
	ds_read_b64_tr_b16 v[44:45], v2 offset:31744
	ds_read_b64_tr_b16 v[46:47], v2 offset:32256
	v_add_f32_e32 v2, v50, v136
	v_add_f32_e32 v2, v51, v2
	v_add_f32_e32 v2, 0, v2
	v_cvt_pk_bf16_f32 v118, v48, v49
	v_cvt_pk_bf16_f32 v119, v50, v51
	v_mfma_f32_32x32x16_bf16 v[68:83], v[132:135], v[100:103], v[68:83]
	v_lshl_add_u64 v[48:49], v[170:171], 0, s[94:95]
	s_add_i32 s11, s12, s36
	s_mov_b32 s12, m0
	s_mov_b32 m0, s11
	s_nop 0
	global_load_lds_dwordx4 v[48:49], off
	s_mov_b32 m0, s12
	v_lshl_add_u64 v[48:49], v[168:169], 0, s[94:95]
	s_add_i32 s11, s13, s38
	s_mov_b32 s12, m0
	s_mov_b32 m0, s11
	s_nop 0
	global_load_lds_dwordx4 v[48:49], off
	s_mov_b32 m0, s12
	v_add_f32_e32 v2, v176, v2
	s_waitcnt lgkmcnt(14)
	v_mfma_f32_32x32x16_bf16 v[4:19], v[128:131], v[172:175], v[4:19]
	v_exp_f32_e32 v84, v84
	v_exp_f32_e32 v85, v85
	v_exp_f32_e32 v86, v86
	v_exp_f32_e32 v87, v87
	s_waitcnt lgkmcnt(12)
	v_mfma_f32_32x32x16_bf16 v[20:35], v[128:131], v[52:55], v[20:35]
	v_exp_f32_e32 v88, v88
	v_exp_f32_e32 v89, v89
	v_exp_f32_e32 v90, v90
	v_exp_f32_e32 v91, v91
	v_add_u32_e32 v52, s91, v253
	ds_read_b128 v[48:51], v52
	ds_read_b128 v[136:139], v52 offset:512
	s_waitcnt lgkmcnt(12)
	v_mfma_f32_32x32x16_bf16 v[4:19], v[124:127], v[56:59], v[4:19]
	v_exp_f32_e32 v92, v92
	v_exp_f32_e32 v93, v93
	v_exp_f32_e32 v94, v94
	v_exp_f32_e32 v95, v95
	ds_read_b128 v[140:143], v52 offset:2048
	ds_read_b128 v[144:147], v52 offset:2560
	s_waitcnt lgkmcnt(12)
	v_mfma_f32_32x32x16_bf16 v[20:35], v[124:127], v[60:63], v[20:35]
	v_exp_f32_e32 v96, v96
	v_exp_f32_e32 v97, v97
	v_exp_f32_e32 v98, v98
	v_exp_f32_e32 v99, v99
	ds_read_b128 v[148:151], v52 offset:4096
	ds_read_b128 v[152:155], v52 offset:4608
	s_waitcnt lgkmcnt(12)
	v_mfma_f32_32x32x16_bf16 v[4:19], v[120:123], v[64:67], v[4:19]
	v_exp_f32_e32 v68, v68
	v_exp_f32_e32 v69, v69
	v_exp_f32_e32 v70, v70
	v_exp_f32_e32 v71, v71
	ds_read_b128 v[156:159], v52 offset:6144
	ds_read_b128 v[132:135], v52 offset:6656
	s_waitcnt lgkmcnt(12)
	v_mfma_f32_32x32x16_bf16 v[20:35], v[120:123], v[36:39], v[20:35]
	v_exp_f32_e32 v72, v72
	v_exp_f32_e32 v73, v73
	v_exp_f32_e32 v74, v74
	v_exp_f32_e32 v75, v75
	s_waitcnt lgkmcnt(10)
	v_mfma_f32_32x32x16_bf16 v[4:19], v[116:119], v[40:43], v[4:19]
	v_exp_f32_e32 v76, v76
	v_exp_f32_e32 v77, v77
	v_exp_f32_e32 v78, v78
	v_exp_f32_e32 v79, v79
	s_waitcnt lgkmcnt(8)
	v_mfma_f32_32x32x16_bf16 v[20:35], v[116:119], v[44:47], v[20:35]
	v_exp_f32_e32 v80, v80
	v_exp_f32_e32 v81, v81
	v_exp_f32_e32 v82, v82
	v_exp_f32_e32 v83, v83
	s_add_i32 s11, s91, 0x2000
	s_cmpk_lg_i32 s91, 0x4000
	s_waitcnt vmcnt(2) lgkmcnt(0)
	s_barrier
	s_cselect_b32 s12, s11, 0
	s_add_i32 s11, s13, 0x2000
	s_cmpk_lg_i32 s13, 0x4000
	s_cselect_b32 s39, s11, 0
	v_add_u32_e32 v172, s9, v242
	ds_read_b64_tr_b16 v[160:161], v172 offset:24576
	ds_read_b64_tr_b16 v[162:163], v172 offset:25088
	s_waitcnt lgkmcnt(9)
	v_mfma_f32_32x32x16_bf16 v[52:67], v[48:51], v[112:115], 0
	v_add_f32_e32 v36, v84, v85
	v_add_f32_e32 v36, v86, v36
	v_add_f32_e32 v36, v87, v36
	v_add_f32_e32 v36, v88, v36
	v_add_f32_e32 v36, v89, v36
	v_cvt_pk_bf16_f32 v128, v84, v85
	v_cvt_pk_bf16_f32 v129, v86, v87
	ds_read_b64_tr_b16 v[84:85], v172 offset:28672
	ds_read_b64_tr_b16 v[86:87], v172 offset:29184
	v_add_f32_e32 v36, v90, v36
	v_add_f32_e32 v36, v91, v36
	v_add_f32_e32 v36, v92, v36
	v_add_f32_e32 v116, v93, v36
	s_waitcnt lgkmcnt(10)
	v_mfma_f32_32x32x16_bf16 v[36:51], v[136:139], v[112:115], 0
	v_cvt_pk_bf16_f32 v130, v88, v89
	v_cvt_pk_bf16_f32 v131, v90, v91
	ds_read_b64_tr_b16 v[88:89], v172 offset:25600
	ds_read_b64_tr_b16 v[90:91], v172 offset:26112
	s_waitcnt lgkmcnt(11)
	v_mfma_f32_32x32x16_bf16 v[52:67], v[140:143], v[108:111], v[52:67]
	v_add_f32_e32 v116, v94, v116
	v_add_f32_e32 v116, v95, v116
	v_add_f32_e32 v116, v96, v116
	v_add_f32_e32 v116, v97, v116
	v_cvt_pk_bf16_f32 v124, v92, v93
	v_cvt_pk_bf16_f32 v125, v94, v95
	ds_read_b64_tr_b16 v[92:93], v172 offset:29696
	ds_read_b64_tr_b16 v[94:95], v172 offset:30208
	s_waitcnt lgkmcnt(12)
	v_mfma_f32_32x32x16_bf16 v[36:51], v[144:147], v[108:111], v[36:51]
	v_add_f32_e32 v116, v98, v116
	v_add_f32_e32 v116, v99, v116
	v_add_f32_e32 v116, v68, v116
	v_add_f32_e32 v116, v69, v116
	v_cvt_pk_bf16_f32 v126, v96, v97
	v_cvt_pk_bf16_f32 v127, v98, v99
	ds_read_b64_tr_b16 v[96:97], v172 offset:26624
	ds_read_b64_tr_b16 v[98:99], v172 offset:27136
	s_waitcnt lgkmcnt(13)
	v_mfma_f32_32x32x16_bf16 v[52:67], v[148:151], v[104:107], v[52:67]
	v_add_f32_e32 v116, v70, v116
	v_add_f32_e32 v116, v71, v116
	v_add_f32_e32 v116, v72, v116
	v_add_f32_e32 v116, v73, v116
	v_cvt_pk_bf16_f32 v120, v68, v69
	v_cvt_pk_bf16_f32 v121, v70, v71
	ds_read_b64_tr_b16 v[68:69], v172 offset:30720
	ds_read_b64_tr_b16 v[70:71], v172 offset:31232
	s_waitcnt lgkmcnt(14)
	v_mfma_f32_32x32x16_bf16 v[36:51], v[152:155], v[104:107], v[36:51]
	v_add_f32_e32 v116, v74, v116
	v_add_f32_e32 v116, v75, v116
	v_add_f32_e32 v116, v76, v116
	v_add_f32_e32 v116, v77, v116
	v_cvt_pk_bf16_f32 v122, v72, v73
	v_cvt_pk_bf16_f32 v123, v74, v75
	ds_read_b64_tr_b16 v[72:73], v172 offset:27648
	ds_read_b64_tr_b16 v[74:75], v172 offset:28160
	s_waitcnt lgkmcnt(14)
	v_mfma_f32_32x32x16_bf16 v[52:67], v[156:159], v[100:103], v[52:67]
	v_add_f32_e32 v116, v78, v116
	v_add_f32_e32 v116, v79, v116
	v_add_f32_e32 v116, v80, v116
	v_add_f32_e32 v136, v81, v116
	v_cvt_pk_bf16_f32 v116, v76, v77
	v_cvt_pk_bf16_f32 v117, v78, v79
	ds_read_b64_tr_b16 v[76:77], v172 offset:31744
	ds_read_b64_tr_b16 v[78:79], v172 offset:32256
	v_mfma_f32_32x32x16_bf16 v[36:51], v[132:135], v[100:103], v[36:51]
	v_add_f32_e32 v118, v82, v136
	v_add_f32_e32 v118, v83, v118
	v_add_f32_e32 v132, 0, v118
	v_cvt_pk_bf16_f32 v118, v80, v81
	v_cvt_pk_bf16_f32 v119, v82, v83
	s_add_i32 s9, s91, s36
	s_mov_b32 s11, m0
	s_mov_b32 m0, s9
	s_nop 0
	global_load_lds_dwordx4 v[170:171], off
	s_mov_b32 m0, s11
	s_add_i32 s9, s39, s38
	s_mov_b32 s11, m0
	s_mov_b32 m0, s9
	s_nop 0
	global_load_lds_dwordx4 v[168:169], off
	s_mov_b32 m0, s11
	v_add_f32_e32 v176, v2, v132
	s_waitcnt lgkmcnt(14)
	v_mfma_f32_32x32x16_bf16 v[4:19], v[128:131], v[160:163], v[4:19]
	v_exp_f32_e32 v52, v52
	v_exp_f32_e32 v53, v53
	v_exp_f32_e32 v54, v54
	v_exp_f32_e32 v55, v55
	s_waitcnt lgkmcnt(12)
	v_mfma_f32_32x32x16_bf16 v[20:35], v[128:131], v[84:87], v[20:35]
	v_exp_f32_e32 v56, v56
	v_exp_f32_e32 v57, v57
	v_exp_f32_e32 v58, v58
	v_exp_f32_e32 v59, v59
	v_add_u32_e32 v2, s12, v253
	ds_read_b128 v[160:163], v2
	ds_read_b128 v[152:155], v2 offset:512
	s_waitcnt lgkmcnt(12)
	v_mfma_f32_32x32x16_bf16 v[4:19], v[124:127], v[88:91], v[4:19]
	v_exp_f32_e32 v60, v60
	v_exp_f32_e32 v61, v61
	v_exp_f32_e32 v62, v62
	v_exp_f32_e32 v63, v63
	ds_read_b128 v[156:159], v2 offset:2048
	ds_read_b128 v[148:151], v2 offset:2560
	s_waitcnt lgkmcnt(12)
	v_mfma_f32_32x32x16_bf16 v[20:35], v[124:127], v[92:95], v[20:35]
	v_exp_f32_e32 v64, v64
	v_exp_f32_e32 v65, v65
	v_exp_f32_e32 v66, v66
	v_exp_f32_e32 v67, v67
	ds_read_b128 v[144:147], v2 offset:4096
	ds_read_b128 v[140:143], v2 offset:4608
	s_waitcnt lgkmcnt(12)
	v_mfma_f32_32x32x16_bf16 v[4:19], v[120:123], v[96:99], v[4:19]
	v_exp_f32_e32 v36, v36
	v_exp_f32_e32 v37, v37
	v_exp_f32_e32 v38, v38
	v_exp_f32_e32 v39, v39
	ds_read_b128 v[136:139], v2 offset:6144
	ds_read_b128 v[132:135], v2 offset:6656
	s_waitcnt lgkmcnt(12)
	v_mfma_f32_32x32x16_bf16 v[20:35], v[120:123], v[68:71], v[20:35]
	v_exp_f32_e32 v40, v40
	v_exp_f32_e32 v41, v41
	v_exp_f32_e32 v42, v42
	v_exp_f32_e32 v43, v43
	s_waitcnt lgkmcnt(10)
	v_mfma_f32_32x32x16_bf16 v[4:19], v[116:119], v[72:75], v[4:19]
	v_exp_f32_e32 v44, v44
	v_exp_f32_e32 v45, v45
	v_exp_f32_e32 v46, v46
	v_exp_f32_e32 v47, v47
	s_waitcnt lgkmcnt(8)
	v_mfma_f32_32x32x16_bf16 v[20:35], v[116:119], v[76:79], v[20:35]
	v_exp_f32_e32 v48, v48
	v_exp_f32_e32 v49, v49
	v_exp_f32_e32 v50, v50
	v_exp_f32_e32 v51, v51
	s_add_i32 s9, s12, 0x2000
	s_cmpk_lg_i32 s12, 0x4000
	s_cselect_b32 s91, s9, 0
	s_add_i32 s9, s39, 0x2000
	s_waitcnt vmcnt(2) lgkmcnt(0)
	s_barrier
	s_cmpk_lg_i32 s39, 0x4000
	s_cselect_b32 s13, s9, 0
	s_add_i32 s24, s24, 2
	v_lshl_add_u64 v[168:169], v[168:169], 0, s[92:93]
	v_lshl_add_u64 v[170:171], v[170:171], 0, s[92:93]
	s_cmp_ge_u32 s24, s77
	s_mov_b32 s11, s40
	s_cbranch_scc0 .LBB0_910
	s_add_i32 s24, s8, -3
	s_ashr_i32 s11, s10, 31
	s_add_i32 s8, s24, 1
	s_cmp_ge_u32 s8, s77
	s_cbranch_scc0 .LBB0_962

.LBB0_1054:
	v_readlane_b32 s74, v255, 18
	v_readlane_b32 s6, v255, 27
	v_readlane_b32 s75, v255, 19
	v_readlane_b32 s7, v255, 28
	s_waitcnt vmcnt(0) lgkmcnt(0)
	s_barrier
	s_setprio 0
